# P5 epilogue de-serialised: x loads run six steps ahead in free fragment registers with counted waits (was load-wait-add-store ladder)
# baseline (speedup 1.0000x reference)
.LBB0_525:
	v_lshl_add_u32 v138, s71, 8, v145
	v_lshl_or_b32 v136, s70, 8, v146
	s_andn2_b64 vcc, exec, s[4:5]
	s_mov_b64 s[4:5], -1
	v_lshl_add_u32 v134, v138, 11, v136
	v_lshlrev_b32_e32 v135, 2, v134
	v_lshlrev_b32_e32 v137, 1, v134
	v_mov_b32_e32 v152, v135
	global_load_dwordx4 v[164:167], v152, s[36:37]
	global_load_dwordx4 v[168:171], v152, s[36:37] offset:16
	global_load_dwordx4 v[172:175], v152, s[36:37] offset:512
	global_load_dwordx4 v[176:179], v152, s[36:37] offset:528
	v_add_u32_e32 v153, 0x20000, v135
	global_load_dwordx4 v[180:183], v153, s[36:37]
	global_load_dwordx4 v[184:187], v153, s[36:37] offset:16
	global_load_dwordx4 v[188:191], v153, s[36:37] offset:512
	global_load_dwordx4 v[192:195], v153, s[36:37] offset:528
	v_add_u32_e32 v154, 0x40000, v135
	global_load_dwordx4 v[198:201], v154, s[36:37]
	global_load_dwordx4 v[202:205], v154, s[36:37] offset:16
	global_load_dwordx4 v[206:209], v154, s[36:37] offset:512
	global_load_dwordx4 v[210:213], v154, s[36:37] offset:528
	s_waitcnt vmcnt(10)
	v_pk_add_f32 v[126:127], v[126:127], v[164:165]
	v_pk_add_f32 v[128:129], v[128:129], v[166:167]
	v_pk_add_f32 v[122:123], v[122:123], v[168:169]
	v_pk_add_f32 v[124:125], v[124:125], v[170:171]
	v_mov_b32_e32 v160, v137
	v_cvt_pk_bf16_f32 v126, v126, v127
	v_cvt_pk_bf16_f32 v127, v128, v129
	v_cvt_pk_bf16_f32 v128, v122, v123
	v_cvt_pk_bf16_f32 v129, v124, v125
	global_store_dwordx4 v160, v[126:129], s[12:13]
	v_add_u32_e32 v155, 0x60000, v135
	global_load_dwordx4 v[164:167], v155, s[36:37]
	global_load_dwordx4 v[168:171], v155, s[36:37] offset:16
	s_waitcnt vmcnt(11)
	v_pk_add_f32 v[118:119], v[118:119], v[172:173]
	v_pk_add_f32 v[120:121], v[120:121], v[174:175]
	v_pk_add_f32 v[114:115], v[114:115], v[176:177]
	v_pk_add_f32 v[116:117], v[116:117], v[178:179]
	v_mov_b32_e32 v161, v137
	v_cvt_pk_bf16_f32 v118, v118, v119
	v_cvt_pk_bf16_f32 v119, v120, v121
	v_cvt_pk_bf16_f32 v120, v114, v115
	v_cvt_pk_bf16_f32 v121, v116, v117
	global_store_dwordx4 v161, v[118:121], s[12:13] offset:256
	global_load_dwordx4 v[172:175], v155, s[36:37] offset:512
	global_load_dwordx4 v[176:179], v155, s[36:37] offset:528
	s_waitcnt vmcnt(12)
	v_pk_add_f32 v[110:111], v[110:111], v[180:181]
	v_pk_add_f32 v[112:113], v[112:113], v[182:183]
	v_pk_add_f32 v[106:107], v[106:107], v[184:185]
	v_pk_add_f32 v[108:109], v[108:109], v[186:187]
	v_add_u32_e32 v160, 0x10000, v137
	v_cvt_pk_bf16_f32 v110, v110, v111
	v_cvt_pk_bf16_f32 v111, v112, v113
	v_cvt_pk_bf16_f32 v112, v106, v107
	v_cvt_pk_bf16_f32 v113, v108, v109
	global_store_dwordx4 v160, v[110:113], s[12:13]
	v_add_u32_e32 v156, 0x100000, v135
	global_load_dwordx4 v[180:183], v156, s[36:37]
	global_load_dwordx4 v[184:187], v156, s[36:37] offset:16
	s_waitcnt vmcnt(13)
	v_pk_add_f32 v[102:103], v[102:103], v[188:189]
	v_pk_add_f32 v[104:105], v[104:105], v[190:191]
	v_pk_add_f32 v[98:99], v[98:99], v[192:193]
	v_pk_add_f32 v[100:101], v[100:101], v[194:195]
	v_add_u32_e32 v161, 0x10000, v137
	v_cvt_pk_bf16_f32 v102, v102, v103
	v_cvt_pk_bf16_f32 v103, v104, v105
	v_cvt_pk_bf16_f32 v104, v98, v99
	v_cvt_pk_bf16_f32 v105, v100, v101
	global_store_dwordx4 v161, v[102:105], s[12:13] offset:256
	global_load_dwordx4 v[188:191], v156, s[36:37] offset:512
	global_load_dwordx4 v[192:195], v156, s[36:37] offset:528
	s_waitcnt vmcnt(14)
	v_pk_add_f32 v[94:95], v[94:95], v[198:199]
	v_pk_add_f32 v[96:97], v[96:97], v[200:201]
	v_pk_add_f32 v[90:91], v[90:91], v[202:203]
	v_pk_add_f32 v[92:93], v[92:93], v[204:205]
	v_add_u32_e32 v160, 0x20000, v137
	v_cvt_pk_bf16_f32 v94, v94, v95
	v_cvt_pk_bf16_f32 v95, v96, v97
	v_cvt_pk_bf16_f32 v96, v90, v91
	v_cvt_pk_bf16_f32 v97, v92, v93
	global_store_dwordx4 v160, v[94:97], s[12:13]
	v_add_u32_e32 v157, 0x120000, v135
	global_load_dwordx4 v[198:201], v157, s[36:37]
	global_load_dwordx4 v[202:205], v157, s[36:37] offset:16
	s_waitcnt vmcnt(15)
	v_pk_add_f32 v[86:87], v[86:87], v[206:207]
	v_pk_add_f32 v[88:89], v[88:89], v[208:209]
	v_pk_add_f32 v[82:83], v[82:83], v[210:211]
	v_pk_add_f32 v[84:85], v[84:85], v[212:213]
	v_add_u32_e32 v161, 0x20000, v137
	v_cvt_pk_bf16_f32 v86, v86, v87
	v_cvt_pk_bf16_f32 v87, v88, v89
	v_cvt_pk_bf16_f32 v88, v82, v83
	v_cvt_pk_bf16_f32 v89, v84, v85
	global_store_dwordx4 v161, v[86:89], s[12:13] offset:256
	global_load_dwordx4 v[206:209], v157, s[36:37] offset:512
	global_load_dwordx4 v[210:213], v157, s[36:37] offset:528
	s_waitcnt vmcnt(15)
	v_pk_add_f32 v[78:79], v[78:79], v[164:165]
	v_pk_add_f32 v[80:81], v[80:81], v[166:167]
	v_pk_add_f32 v[74:75], v[74:75], v[168:169]
	v_pk_add_f32 v[76:77], v[76:77], v[170:171]
	v_add_u32_e32 v160, 0x30000, v137
	v_cvt_pk_bf16_f32 v78, v78, v79
	v_cvt_pk_bf16_f32 v79, v80, v81
	v_cvt_pk_bf16_f32 v80, v74, v75
	v_cvt_pk_bf16_f32 v81, v76, v77
	global_store_dwordx4 v160, v[78:81], s[12:13]
	v_add_u32_e32 v158, 0x140000, v135
	global_load_dwordx4 v[164:167], v158, s[36:37]
	global_load_dwordx4 v[168:171], v158, s[36:37] offset:16
	s_waitcnt vmcnt(15)
	v_pk_add_f32 v[70:71], v[70:71], v[172:173]
	v_pk_add_f32 v[72:73], v[72:73], v[174:175]
	v_pk_add_f32 v[66:67], v[66:67], v[176:177]
	v_pk_add_f32 v[68:69], v[68:69], v[178:179]
	v_add_u32_e32 v161, 0x30000, v137
	v_cvt_pk_bf16_f32 v70, v70, v71
	v_cvt_pk_bf16_f32 v71, v72, v73
	v_cvt_pk_bf16_f32 v72, v66, v67
	v_cvt_pk_bf16_f32 v73, v68, v69
	global_store_dwordx4 v161, v[70:73], s[12:13] offset:256
	global_load_dwordx4 v[172:175], v158, s[36:37] offset:512
	global_load_dwordx4 v[176:179], v158, s[36:37] offset:528
	s_waitcnt vmcnt(15)
	v_pk_add_f32 v[62:63], v[62:63], v[180:181]
	v_pk_add_f32 v[64:65], v[64:65], v[182:183]
	v_pk_add_f32 v[58:59], v[58:59], v[184:185]
	v_pk_add_f32 v[60:61], v[60:61], v[186:187]
	v_add_u32_e32 v160, 0x80000, v137
	v_cvt_pk_bf16_f32 v62, v62, v63
	v_cvt_pk_bf16_f32 v63, v64, v65
	v_cvt_pk_bf16_f32 v64, v58, v59
	v_cvt_pk_bf16_f32 v65, v60, v61
	global_store_dwordx4 v160, v[62:65], s[12:13]
	v_add_u32_e32 v159, 0x160000, v135
	global_load_dwordx4 v[180:183], v159, s[36:37]
	global_load_dwordx4 v[184:187], v159, s[36:37] offset:16
	s_waitcnt vmcnt(15)
	v_pk_add_f32 v[54:55], v[54:55], v[188:189]
	v_pk_add_f32 v[56:57], v[56:57], v[190:191]
	v_pk_add_f32 v[50:51], v[50:51], v[192:193]
	v_pk_add_f32 v[52:53], v[52:53], v[194:195]
	v_add_u32_e32 v161, 0x80000, v137
	v_cvt_pk_bf16_f32 v54, v54, v55
	v_cvt_pk_bf16_f32 v55, v56, v57
	v_cvt_pk_bf16_f32 v56, v50, v51
	v_cvt_pk_bf16_f32 v57, v52, v53
	global_store_dwordx4 v161, v[54:57], s[12:13] offset:256
	global_load_dwordx4 v[188:191], v159, s[36:37] offset:512
	global_load_dwordx4 v[192:195], v159, s[36:37] offset:528
	s_waitcnt vmcnt(15)
	v_pk_add_f32 v[46:47], v[46:47], v[198:199]
	v_pk_add_f32 v[48:49], v[48:49], v[200:201]
	v_pk_add_f32 v[42:43], v[42:43], v[202:203]
	v_pk_add_f32 v[44:45], v[44:45], v[204:205]
	v_add_u32_e32 v160, 0x90000, v137
	v_cvt_pk_bf16_f32 v46, v46, v47
	v_cvt_pk_bf16_f32 v47, v48, v49
	v_cvt_pk_bf16_f32 v48, v42, v43
	v_cvt_pk_bf16_f32 v49, v44, v45
	global_store_dwordx4 v160, v[46:49], s[12:13]
	s_waitcnt vmcnt(13)
	v_pk_add_f32 v[30:31], v[30:31], v[206:207]
	v_pk_add_f32 v[32:33], v[32:33], v[208:209]
	v_pk_add_f32 v[26:27], v[26:27], v[210:211]
	v_pk_add_f32 v[28:29], v[28:29], v[212:213]
	v_add_u32_e32 v161, 0x90000, v137
	v_cvt_pk_bf16_f32 v30, v30, v31
	v_cvt_pk_bf16_f32 v31, v32, v33
	v_cvt_pk_bf16_f32 v32, v26, v27
	v_cvt_pk_bf16_f32 v33, v28, v29
	global_store_dwordx4 v161, v[30:33], s[12:13] offset:256
	s_waitcnt vmcnt(11)
	v_pk_add_f32 v[22:23], v[22:23], v[164:165]
	v_pk_add_f32 v[24:25], v[24:25], v[166:167]
	v_pk_add_f32 v[18:19], v[18:19], v[168:169]
	v_pk_add_f32 v[20:21], v[20:21], v[170:171]
	v_add_u32_e32 v160, 0xa0000, v137
	v_cvt_pk_bf16_f32 v22, v22, v23
	v_cvt_pk_bf16_f32 v23, v24, v25
	v_cvt_pk_bf16_f32 v24, v18, v19
	v_cvt_pk_bf16_f32 v25, v20, v21
	global_store_dwordx4 v160, v[22:25], s[12:13]
	s_waitcnt vmcnt(9)
	v_pk_add_f32 v[34:35], v[34:35], v[172:173]
	v_pk_add_f32 v[36:37], v[36:37], v[174:175]
	v_pk_add_f32 v[38:39], v[38:39], v[176:177]
	v_pk_add_f32 v[40:41], v[40:41], v[178:179]
	v_add_u32_e32 v161, 0xa0000, v137
	v_cvt_pk_bf16_f32 v34, v34, v35
	v_cvt_pk_bf16_f32 v35, v36, v37
	v_cvt_pk_bf16_f32 v36, v38, v39
	v_cvt_pk_bf16_f32 v37, v40, v41
	global_store_dwordx4 v161, v[34:37], s[12:13] offset:256
	s_waitcnt vmcnt(7)
	v_pk_add_f32 v[6:7], v[6:7], v[180:181]
	v_pk_add_f32 v[8:9], v[8:9], v[182:183]
	v_pk_add_f32 v[2:3], v[2:3], v[184:185]
	v_pk_add_f32 v[4:5], v[4:5], v[186:187]
	v_add_u32_e32 v160, 0xb0000, v137
	v_cvt_pk_bf16_f32 v6, v6, v7
	v_cvt_pk_bf16_f32 v7, v8, v9
	v_cvt_pk_bf16_f32 v8, v2, v3
	v_cvt_pk_bf16_f32 v9, v4, v5
	global_store_dwordx4 v160, v[6:9], s[12:13]
	s_waitcnt vmcnt(5)
	v_pk_add_f32 v[10:11], v[10:11], v[188:189]
	v_pk_add_f32 v[12:13], v[12:13], v[190:191]
	v_pk_add_f32 v[14:15], v[14:15], v[192:193]
	v_pk_add_f32 v[16:17], v[16:17], v[194:195]
	v_add_u32_e32 v161, 0xb0000, v137
	v_cvt_pk_bf16_f32 v10, v10, v11
	v_cvt_pk_bf16_f32 v11, v12, v13
	v_cvt_pk_bf16_f32 v12, v14, v15
	v_cvt_pk_bf16_f32 v13, v16, v17
	global_store_dwordx4 v161, v[10:13], s[12:13] offset:256
	s_cbranch_vccnz .LBB0_514
	s_andn2_b64 vcc, exec, s[0:1]
	s_cbranch_vccnz .LBB0_513
	s_barrier
	s_branch .LBB0_513
